# in-proj GEMM on 184 workgroups (was 180), gate/up conversion on 72
# speedup vs baseline: 1.0007x; 1.0007x over previous
; #define LAS __attribute__((address_space(3)))
; __device__ __forceinline__ void wout_transpose(const Params& p, Frame& F, int gw, int NGW) {
;     LAS unsigned char* tile = F.lds + 16384 + F.wave * 16384;
;     __syncthreads();
;     for (int it = gw; it < (DM / 128) * (DM / 64); it += NGW) {
;         const int nb = it % (DM / 64), kb = it / (DM / 64); p0_transpose_item_bf16(p.in[10], DM, kb * 128, nb * 64, (bf16_t*)(p.ws + WS_WOUT), DM, nb * 64, nullptr, tile, F.lane);
; __global__ void __launch_bounds__(512, 2) hymba_fwd(Params p) {
;     ...
;         const int ng = (F.G == 256) ? NG_GEMM : F.G;
;         if ((int)blockIdx.x < ng) {
;             pg8::Gemm g{(const bf16_t*)(ws + WS_XB), (const bf16_t*)(ws + WS_WIN), DM}; pg8::StaticOrder S; S.init(T_TOK, NPROJ, ng, (int)blockIdx.x);
;             EpiProj E{(bf16_t*)(ws + WS_PROJ), (const float*)(ws + WS_RSTD1)};
;             pg8::gemm_phase<EpiProj, pg8::StaticOrder, false, false, true, false>(ring, g, S, E);
;             if (ng == F.G) { wout_transpose(p, F, (int)blockIdx.x * 8 + F.wave, F.G * 8); moe_weight_convert(p, F, (int)blockIdx.x * 8 + F.wave, F.G * 8, 0, CONV_N_GU); }
;         } else { wout_transpose(p, F, ((int)blockIdx.x - ng) * 8 + F.wave, (F.G - ng) * 8); moe_weight_convert(p, F, ((int)blockIdx.x - ng) * 8 + F.wave, (F.G - ng) * 8, 0, CONV_N_GU); }
.LBB0_145:
	v_readlane_b32 s4, v245, 4
	s_cmp_lt_i32 s4, 2
	s_cselect_b64 s[0:1], -1, 0
	s_and_b64 s[2:3], s[0:1], s[2:3]
	s_andn2_b64 vcc, exec, s[2:3]
	v_readlane_b32 s5, v245, 5
	v_readlane_b32 s6, v245, 6
	v_readlane_b32 s7, v245, 7
	s_cbranch_vccnz .LBB0_233
	s_cmpk_lg_i32 s94, 0x100
	s_cselect_b64 s[12:13], -1, 0
	s_and_b64 s[2:3], s[12:13], exec
	s_cselect_b32 s20, s94, 0xb8
	v_readlane_b32 s2, v245, 18
	s_cmp_ge_i32 s2, s20
	s_mov_b64 s[2:3], -1
	s_cbranch_scc0 .LBB0_182
	v_readlane_b32 s2, v245, 18
	s_sub_i32 s2, s2, s20
	s_lshl_b32 s6, s2, 3
	s_sub_i32 s2, s94, s20
	s_add_i32 s6, s6, s54
	s_lshl_b32 s21, s2, 3
	v_readlane_b32 s56, v245, 39
	s_cmpk_gt_u32 s6, 0x1ff
	v_readlane_b32 s60, v245, 43
	v_readlane_b32 s61, v245, 44
	v_readlane_b32 s62, v245, 45
	v_readlane_b32 s63, v245, 46
	s_barrier
	v_readlane_b32 s57, v245, 40
	v_readlane_b32 s58, v245, 41
	v_readlane_b32 s59, v245, 42
	v_readlane_b32 s64, v245, 47
	v_readlane_b32 s65, v245, 48
	v_readlane_b32 s66, v245, 49
	v_readlane_b32 s67, v245, 50
	v_readlane_b32 s68, v245, 51
	v_readlane_b32 s69, v245, 52
	v_readlane_b32 s70, v245, 53
	v_readlane_b32 s71, v245, 54
	s_cbranch_scc1 .LBB0_150
	s_lshl_b32 s2, s54, 14
	v_lshrrev_b32_e32 v5, 1, v162
	s_add_i32 s4, s2, 0
	v_and_b32_e32 v2, 15, v0
	v_lshrrev_b32_e32 v4, 5, v162
	v_and_b32_e32 v5, 8, v5
	v_lshrrev_b32_e32 v1, 4, v162
	v_lshlrev_b32_e32 v8, 2, v2
	v_mov_b32_e32 v3, 0
	v_add_u32_e32 v5, s4, v5
	v_bitop3_b32 v7, v4, v0, 15 bitop3:0x78
	v_lshlrev_b32_e32 v9, 10, v2
	v_bitop3_b32 v10, v4, v2, 2 bitop3:0x36
	v_bitop3_b32 v11, v4, v2, 4 bitop3:0x36
	v_bitop3_b32 v12, v4, v2, 6 bitop3:0x36
	v_bitop3_b32 v13, v4, v2, 8 bitop3:0x36
	v_bitop3_b32 v14, v4, v2, 10 bitop3:0x36
	v_bitop3_b32 v15, v4, v2, 12 bitop3:0x36
	v_bitop3_b32 v4, v4, v2, 14 bitop3:0x36
	v_lshlrev_b32_e32 v2, 4, v2
	v_lshl_add_u32 v7, v7, 4, v5
	v_lshl_add_u32 v10, v10, 4, v5
	v_lshl_add_u32 v11, v11, 4, v5
	v_lshl_add_u32 v12, v12, 4, v5
	v_lshl_add_u32 v13, v13, 4, v5
	v_lshl_add_u32 v14, v14, 4, v5
	v_lshl_add_u32 v15, v15, 4, v5
	v_lshl_add_u32 v16, v4, 4, v5
	v_lshl_add_u64 v[4:5], s[96:97], 0, v[2:3]
	v_lshl_add_u32 v17, v1, 8, s4
	v_lshlrev_b32_e32 v2, 4, v0
	v_mov_b32_e32 v20, 0xf0
	s_movk_i32 s4, 0x80
	v_bitop3_b32 v35, v2, s4, v20 bitop3:0x6c
	s_movk_i32 s4, 0x90
	v_bitop3_b32 v37, v2, s4, v20 bitop3:0x6c
	s_movk_i32 s4, 0xa0
	s_mov_b64 s[2:3], 0x31000000
	v_bitop3_b32 v39, v2, s4, v20 bitop3:0x6c
	s_movk_i32 s4, 0xb0
	v_lshl_add_u64 v[4:5], v[4:5], 0, s[2:3]
	s_movk_i32 s2, 0x50
	v_bitop3_b32 v41, v2, s4, v20 bitop3:0x6c
	s_movk_i32 s4, 0xc0
	v_bitop3_b32 v29, v2, s2, v20 bitop3:0x6c
	s_movk_i32 s2, 0x60
	v_bitop3_b32 v43, v2, s4, v20 bitop3:0x6c
	s_movk_i32 s4, 0xd0
	s_movk_i32 s3, 0xf0
	v_bitop3_b32 v31, v2, s2, v20 bitop3:0x6c
	s_movk_i32 s2, 0x70
	v_bitop3_b32 v45, v2, s4, v20 bitop3:0x6c
	s_movk_i32 s4, 0xe0
	v_and_b32_e32 v18, 0xf0, v2
	v_add_u32_e32 v19, 0x400, v17
	v_bitop3_b32 v21, v2, 16, v20 bitop3:0x6c
	v_add_u32_e32 v22, 0x800, v17
	v_bitop3_b32 v23, v2, 32, v20 bitop3:0x6c
	v_add_u32_e32 v24, 0xc00, v17
	v_bitop3_b32 v25, v2, 48, v20 bitop3:0x6c
	v_add_u32_e32 v26, 0x1000, v17
	v_bitop3_b32 v27, v2, 64, v20 bitop3:0x6c
	v_add_u32_e32 v28, 0x1400, v17
	v_add_u32_e32 v30, 0x1800, v17
	v_add_u32_e32 v32, 0x1c00, v17
	v_bitop3_b32 v33, v2, s2, v20 bitop3:0x6c
	v_add_u32_e32 v34, 0x2000, v17
	v_add_u32_e32 v36, 0x2400, v17
	v_add_u32_e32 v38, 0x2800, v17
	v_add_u32_e32 v40, 0x2c00, v17
	v_add_u32_e32 v42, 0x3000, v17
	v_add_u32_e32 v44, 0x3400, v17
	v_add_u32_e32 v46, 0x3800, v17
	v_bitop3_b32 v47, v2, s4, v20 bitop3:0x6c
	v_add_u32_e32 v48, 0x3c00, v17
	v_bitop3_b32 v49, v2, s3, v2 bitop3:0xc
	v_add_u32_e32 v50, v7, v9
	v_add_u32_e32 v51, v10, v9
	v_add_u32_e32 v52, v11, v9
	v_add_u32_e32 v53, v12, v9
	v_add_u32_e32 v54, v13, v9
	v_add_u32_e32 v55, v14, v9
	v_add_u32_e32 v56, v15, v9
	v_add_u32_e32 v57, v16, v9
	v_lshlrev_b32_e32 v6, 2, v1
	s_movk_i32 s2, 0x2000
	s_lshl_b32 s3, s6, 6
	s_lshl_b32 s4, s21, 6
	v_lshlrev_b32_e32 v2, 2, v8
	s_movk_i32 s5, 0x4000
	s_movk_i32 s7, 0x6000
	s_mov_b32 s8, 0x20000
	s_mov_b32 s9, 0x22000
	s_mov_b32 s10, 0x24000
	s_mov_b32 s11, 0x26000
	s_mov_b32 s14, 0x40000
	s_mov_b32 s15, 0x42000
	s_mov_b32 s16, 0x44000
	s_mov_b32 s17, 0x46000
	s_mov_b32 s18, 0x60000
	s_mov_b32 s19, 0x62000
	s_mov_b32 s22, 0x64000
	s_mov_b32 s23, 0x66000
	s_mov_b32 s24, 0x80000
	s_mov_b32 s25, 0x82000
	s_mov_b32 s26, 0x84000
	s_mov_b32 s27, 0x86000
	s_mov_b32 s28, 0xa0000
	s_mov_b32 s29, 0xa2000
	s_mov_b32 s30, 0xa4000
	s_mov_b32 s31, 0xa6000
	s_mov_b32 s33, 0xc0000
	s_mov_b32 s34, 0xc2000
	s_mov_b32 s35, 0xc4000
	s_mov_b32 s36, 0xc6000
	s_mov_b32 s37, 0xe0000
	s_mov_b32 s38, 0xe2000
	s_mov_b32 s39, 0xe4000
	s_mov_b32 s40, 0xe6000
	v_add_u32_e32 v7, v17, v18
	v_add_u32_e32 v8, v19, v21
	v_add_u32_e32 v9, v22, v23
	v_add_u32_e32 v10, v24, v25
	v_add_u32_e32 v11, v26, v27
	v_add_u32_e32 v12, v28, v29
	v_add_u32_e32 v13, v30, v31
	v_add_u32_e32 v14, v32, v33
	v_add_u32_e32 v15, v34, v35
	v_add_u32_e32 v16, v36, v37
	v_add_u32_e32 v17, v38, v39
	v_add_u32_e32 v18, v40, v41
	v_add_u32_e32 v19, v42, v43
	v_add_u32_e32 v20, v44, v45
	v_add_u32_e32 v21, v46, v47
	v_add_u32_e32 v22, v48, v49
	v_add_u32_e32 v23, 0x4000, v50
	v_add_u32_e32 v24, 0x4000, v51
	v_add_u32_e32 v25, 0x4000, v52
	v_add_u32_e32 v26, 0x4000, v53
	v_add_u32_e32 v27, 0x4000, v54
	v_add_u32_e32 v28, 0x4000, v55
	v_add_u32_e32 v29, 0x4000, v56
	v_add_u32_e32 v30, 0x4000, v57
	s_mov_b32 s41, s6
